# prep: bq.bk (t0) computed by an idle wave of an early block with a DPP wave reduce; the former last block exits at once
# baseline (speedup 1.0000x reference)
.Lremap_b:
	s_cmpk_lt_u32 s2, 0x188
	s_cbranch_scc1 .Lremap_c
	s_endpgm
.Lremap_c:
	s_addk_i32 s2, 0xff78

.LBB0_30:
	s_cmpk_eq_u32 s2, 0x140
	s_cbranch_scc0 .Lt0_skip
	v_readfirstlane_b32 s9, v0
	s_lshr_b32 s9, s9, 6
	s_cmp_eq_u32 s9, 3
	s_cbranch_scc0 .Lt0_skip
	s_load_dwordx2 s[12:13], s[0:1], 0x8
	s_load_dwordx2 s[14:15], s[0:1], 0x18
	s_load_dwordx2 s[10:11], s[0:1], 0x58
	v_and_b32_e32 v1, 63, v0
	v_lshlrev_b32_e32 v1, 4, v1
	s_waitcnt lgkmcnt(0)
	global_load_dwordx4 v[2:5], v1, s[12:13]
	global_load_dwordx4 v[6:9], v1, s[14:15]
	s_waitcnt vmcnt(0)
	v_mul_f32_e32 v2, v2, v6
	v_fmac_f32_e32 v2, v3, v7
	v_fmac_f32_e32 v2, v4, v8
	v_fmac_f32_e32 v2, v5, v9
	s_nop 1
	v_add_f32_dpp v2, v2, v2 quad_perm:[1,0,3,2] row_mask:0xf bank_mask:0xf
	s_nop 1
	v_add_f32_dpp v2, v2, v2 quad_perm:[2,3,0,1] row_mask:0xf bank_mask:0xf
	s_nop 1
	v_add_f32_dpp v2, v2, v2 row_half_mirror row_mask:0xf bank_mask:0xf
	s_nop 1
	v_add_f32_dpp v2, v2, v2 row_mirror row_mask:0xf bank_mask:0xf
	s_nop 1
	v_add_f32_dpp v2, v2, v2 row_bcast:15 row_mask:0xa bank_mask:0xf
	s_nop 1
	v_add_f32_dpp v2, v2, v2 row_bcast:31 row_mask:0xc bank_mask:0xf
	s_nop 1
	v_readlane_b32 s9, v2, 63
	v_mov_b32_e32 v1, 0
	s_nop 3
	v_mov_b32_e32 v2, s9
	global_store_dword v1, v2, s[10:11]
